# P6 top-4 scan software-pipelined and branch-free (same comparisons and sum order) + P2 late conv rows issued inside the pool loop
# speedup vs baseline: 1.0081x; 1.0081x over previous
.Lp2_nomask_odd:
	s_waitcnt vmcnt(44)
	v_lshlrev_b32_e32 v196, 16, v0
	v_and_b32_e32 v197, 0xffff0000, v0
	v_lshlrev_b32_e32 v198, 16, v1
	v_and_b32_e32 v199, 0xffff0000, v1
	v_lshlrev_b32_e32 v200, 16, v2
	v_and_b32_e32 v201, 0xffff0000, v2
	v_lshlrev_b32_e32 v202, 16, v3
	v_and_b32_e32 v203, 0xffff0000, v3
	s_waitcnt vmcnt(43)
	v_lshlrev_b32_e32 v188, 16, v4
	v_and_b32_e32 v189, 0xffff0000, v4
	v_lshlrev_b32_e32 v190, 16, v5
	v_and_b32_e32 v191, 0xffff0000, v5
	v_lshlrev_b32_e32 v192, 16, v6
	v_and_b32_e32 v193, 0xffff0000, v6
	v_lshlrev_b32_e32 v194, 16, v7
	v_and_b32_e32 v195, 0xffff0000, v7
	v_pk_add_f32 v[196:197], v[196:197], v[188:189]
	v_pk_add_f32 v[198:199], v[198:199], v[190:191]
	v_pk_add_f32 v[200:201], v[200:201], v[192:193]
	v_pk_add_f32 v[202:203], v[202:203], v[194:195]
	s_waitcnt vmcnt(42)
	v_lshlrev_b32_e32 v188, 16, v8
	v_and_b32_e32 v189, 0xffff0000, v8
	v_lshlrev_b32_e32 v190, 16, v9
	v_and_b32_e32 v191, 0xffff0000, v9
	v_lshlrev_b32_e32 v192, 16, v10
	v_and_b32_e32 v193, 0xffff0000, v10
	v_lshlrev_b32_e32 v194, 16, v11
	v_and_b32_e32 v195, 0xffff0000, v11
	v_pk_add_f32 v[196:197], v[196:197], v[188:189]
	v_pk_add_f32 v[198:199], v[198:199], v[190:191]
	v_pk_add_f32 v[200:201], v[200:201], v[192:193]
	v_pk_add_f32 v[202:203], v[202:203], v[194:195]
	s_waitcnt vmcnt(41)
	v_lshlrev_b32_e32 v188, 16, v12
	v_and_b32_e32 v189, 0xffff0000, v12
	v_lshlrev_b32_e32 v190, 16, v13
	v_and_b32_e32 v191, 0xffff0000, v13
	v_lshlrev_b32_e32 v192, 16, v14
	v_and_b32_e32 v193, 0xffff0000, v14
	v_lshlrev_b32_e32 v194, 16, v15
	v_and_b32_e32 v195, 0xffff0000, v15
	v_pk_add_f32 v[196:197], v[196:197], v[188:189]
	v_pk_add_f32 v[198:199], v[198:199], v[190:191]
	v_pk_add_f32 v[200:201], v[200:201], v[192:193]
	v_pk_add_f32 v[202:203], v[202:203], v[194:195]
	s_waitcnt vmcnt(40)
	v_lshlrev_b32_e32 v188, 16, v16
	v_and_b32_e32 v189, 0xffff0000, v16
	v_lshlrev_b32_e32 v190, 16, v17
	v_and_b32_e32 v191, 0xffff0000, v17
	v_lshlrev_b32_e32 v192, 16, v18
	v_and_b32_e32 v193, 0xffff0000, v18
	v_lshlrev_b32_e32 v194, 16, v19
	v_and_b32_e32 v195, 0xffff0000, v19
	v_pk_add_f32 v[196:197], v[196:197], v[188:189]
	v_pk_add_f32 v[198:199], v[198:199], v[190:191]
	v_pk_add_f32 v[200:201], v[200:201], v[192:193]
	v_pk_add_f32 v[202:203], v[202:203], v[194:195]
	s_waitcnt vmcnt(39)
	v_lshlrev_b32_e32 v188, 16, v20
	v_and_b32_e32 v189, 0xffff0000, v20
	v_lshlrev_b32_e32 v190, 16, v21
	v_and_b32_e32 v191, 0xffff0000, v21
	v_lshlrev_b32_e32 v192, 16, v22
	v_and_b32_e32 v193, 0xffff0000, v22
	v_lshlrev_b32_e32 v194, 16, v23
	v_and_b32_e32 v195, 0xffff0000, v23
	v_pk_add_f32 v[196:197], v[196:197], v[188:189]
	v_pk_add_f32 v[198:199], v[198:199], v[190:191]
	v_pk_add_f32 v[200:201], v[200:201], v[192:193]
	v_pk_add_f32 v[202:203], v[202:203], v[194:195]
	s_waitcnt vmcnt(38)
	v_lshlrev_b32_e32 v188, 16, v24
	v_and_b32_e32 v189, 0xffff0000, v24
	v_lshlrev_b32_e32 v190, 16, v25
	v_and_b32_e32 v191, 0xffff0000, v25
	v_lshlrev_b32_e32 v192, 16, v26
	v_and_b32_e32 v193, 0xffff0000, v26
	v_lshlrev_b32_e32 v194, 16, v27
	v_and_b32_e32 v195, 0xffff0000, v27
	v_pk_add_f32 v[196:197], v[196:197], v[188:189]
	v_pk_add_f32 v[198:199], v[198:199], v[190:191]
	v_pk_add_f32 v[200:201], v[200:201], v[192:193]
	v_pk_add_f32 v[202:203], v[202:203], v[194:195]
	s_waitcnt vmcnt(37)
	v_lshlrev_b32_e32 v188, 16, v28
	v_and_b32_e32 v189, 0xffff0000, v28
	v_lshlrev_b32_e32 v190, 16, v29
	v_and_b32_e32 v191, 0xffff0000, v29
	v_lshlrev_b32_e32 v192, 16, v30
	v_and_b32_e32 v193, 0xffff0000, v30
	v_lshlrev_b32_e32 v194, 16, v31
	v_and_b32_e32 v195, 0xffff0000, v31
	v_pk_add_f32 v[196:197], v[196:197], v[188:189]
	v_pk_add_f32 v[198:199], v[198:199], v[190:191]
	v_pk_add_f32 v[200:201], v[200:201], v[192:193]
	v_pk_add_f32 v[202:203], v[202:203], v[194:195]
	s_waitcnt vmcnt(36)
	v_lshlrev_b32_e32 v180, 16, v32
	v_and_b32_e32 v181, 0xffff0000, v32
	v_lshlrev_b32_e32 v182, 16, v33
	v_and_b32_e32 v183, 0xffff0000, v33
	v_lshlrev_b32_e32 v184, 16, v34
	v_and_b32_e32 v185, 0xffff0000, v34
	v_lshlrev_b32_e32 v186, 16, v35
	v_and_b32_e32 v187, 0xffff0000, v35
	s_waitcnt vmcnt(35)
	v_lshlrev_b32_e32 v188, 16, v36
	v_and_b32_e32 v189, 0xffff0000, v36
	v_lshlrev_b32_e32 v190, 16, v37
	v_and_b32_e32 v191, 0xffff0000, v37
	v_lshlrev_b32_e32 v192, 16, v38
	v_and_b32_e32 v193, 0xffff0000, v38
	v_lshlrev_b32_e32 v194, 16, v39
	v_and_b32_e32 v195, 0xffff0000, v39
	v_pk_add_f32 v[180:181], v[180:181], v[188:189]
	v_pk_add_f32 v[182:183], v[182:183], v[190:191]
	v_pk_add_f32 v[184:185], v[184:185], v[192:193]
	v_pk_add_f32 v[186:187], v[186:187], v[194:195]
	s_waitcnt vmcnt(34)
	v_lshlrev_b32_e32 v188, 16, v40
	v_and_b32_e32 v189, 0xffff0000, v40
	v_lshlrev_b32_e32 v190, 16, v41
	v_and_b32_e32 v191, 0xffff0000, v41
	v_lshlrev_b32_e32 v192, 16, v42
	v_and_b32_e32 v193, 0xffff0000, v42
	v_lshlrev_b32_e32 v194, 16, v43
	v_and_b32_e32 v195, 0xffff0000, v43
	v_pk_add_f32 v[180:181], v[180:181], v[188:189]
	v_pk_add_f32 v[182:183], v[182:183], v[190:191]
	v_pk_add_f32 v[184:185], v[184:185], v[192:193]
	v_pk_add_f32 v[186:187], v[186:187], v[194:195]
	s_waitcnt vmcnt(33)
	v_lshlrev_b32_e32 v188, 16, v44
	v_and_b32_e32 v189, 0xffff0000, v44
	v_lshlrev_b32_e32 v190, 16, v45
	v_and_b32_e32 v191, 0xffff0000, v45
	v_lshlrev_b32_e32 v192, 16, v46
	v_and_b32_e32 v193, 0xffff0000, v46
	v_lshlrev_b32_e32 v194, 16, v47
	v_and_b32_e32 v195, 0xffff0000, v47
	v_pk_add_f32 v[180:181], v[180:181], v[188:189]
	v_pk_add_f32 v[182:183], v[182:183], v[190:191]
	v_pk_add_f32 v[184:185], v[184:185], v[192:193]
	v_pk_add_f32 v[186:187], v[186:187], v[194:195]
	s_waitcnt vmcnt(32)
	v_lshlrev_b32_e32 v188, 16, v48
	v_and_b32_e32 v189, 0xffff0000, v48
	v_lshlrev_b32_e32 v190, 16, v49
	v_and_b32_e32 v191, 0xffff0000, v49
	v_lshlrev_b32_e32 v192, 16, v50
	v_and_b32_e32 v193, 0xffff0000, v50
	v_lshlrev_b32_e32 v194, 16, v51
	v_and_b32_e32 v195, 0xffff0000, v51
	v_pk_add_f32 v[180:181], v[180:181], v[188:189]
	v_pk_add_f32 v[182:183], v[182:183], v[190:191]
	v_pk_add_f32 v[184:185], v[184:185], v[192:193]
	v_pk_add_f32 v[186:187], v[186:187], v[194:195]
	s_waitcnt vmcnt(31)
	v_lshlrev_b32_e32 v188, 16, v52
	v_and_b32_e32 v189, 0xffff0000, v52
	v_lshlrev_b32_e32 v190, 16, v53
	v_and_b32_e32 v191, 0xffff0000, v53
	v_lshlrev_b32_e32 v192, 16, v54
	v_and_b32_e32 v193, 0xffff0000, v54
	v_lshlrev_b32_e32 v194, 16, v55
	v_and_b32_e32 v195, 0xffff0000, v55
	v_pk_add_f32 v[180:181], v[180:181], v[188:189]
	v_pk_add_f32 v[182:183], v[182:183], v[190:191]
	v_pk_add_f32 v[184:185], v[184:185], v[192:193]
	v_pk_add_f32 v[186:187], v[186:187], v[194:195]
	s_waitcnt vmcnt(30)
	v_lshlrev_b32_e32 v188, 16, v56
	v_and_b32_e32 v189, 0xffff0000, v56
	v_lshlrev_b32_e32 v190, 16, v57
	v_and_b32_e32 v191, 0xffff0000, v57
	v_lshlrev_b32_e32 v192, 16, v58
	v_and_b32_e32 v193, 0xffff0000, v58
	v_lshlrev_b32_e32 v194, 16, v59
	v_and_b32_e32 v195, 0xffff0000, v59
	v_pk_add_f32 v[180:181], v[180:181], v[188:189]
	v_pk_add_f32 v[182:183], v[182:183], v[190:191]
	v_pk_add_f32 v[184:185], v[184:185], v[192:193]
	v_pk_add_f32 v[186:187], v[186:187], v[194:195]
	v_pk_fma_f32 v[180:181], v[196:197], v[218:219], v[180:181] op_sel_hi:[1,0,1]
	v_pk_fma_f32 v[182:183], v[198:199], v[218:219], v[182:183] op_sel_hi:[1,0,1]
	v_pk_fma_f32 v[184:185], v[200:201], v[218:219], v[184:185] op_sel_hi:[1,0,1]
	v_pk_fma_f32 v[186:187], v[202:203], v[218:219], v[186:187] op_sel_hi:[1,0,1]
	s_add_i32 s2, s5, 1
	v_min_u32_e32 v217, s2, v219
	v_cvt_f32_u32_e32 v217, v217
	v_rcp_f32_e32 v216, v217
	s_waitcnt vmcnt(29)
	v_lshlrev_b32_e32 v188, 16, v60
	v_and_b32_e32 v189, 0xffff0000, v60
	v_lshlrev_b32_e32 v190, 16, v61
	v_and_b32_e32 v191, 0xffff0000, v61
	v_lshlrev_b32_e32 v192, 16, v62
	v_and_b32_e32 v193, 0xffff0000, v62
	v_lshlrev_b32_e32 v194, 16, v63
	v_and_b32_e32 v195, 0xffff0000, v63
	v_pk_add_f32 v[180:181], v[180:181], v[188:189]
	v_pk_add_f32 v[182:183], v[182:183], v[190:191]
	v_pk_add_f32 v[184:185], v[184:185], v[192:193]
	v_pk_add_f32 v[186:187], v[186:187], v[194:195]
	v_pk_fma_f32 v[196:197], v[180:181], v[216:217], v[188:189] op_sel_hi:[1,0,1] neg_lo:[0,0,1] neg_hi:[0,0,1]
	v_pk_fma_f32 v[198:199], v[182:183], v[216:217], v[190:191] op_sel_hi:[1,0,1] neg_lo:[0,0,1] neg_hi:[0,0,1]
	v_pk_fma_f32 v[200:201], v[184:185], v[216:217], v[192:193] op_sel_hi:[1,0,1] neg_lo:[0,0,1] neg_hi:[0,0,1]
	v_pk_fma_f32 v[202:203], v[186:187], v[216:217], v[194:195] op_sel_hi:[1,0,1] neg_lo:[0,0,1] neg_hi:[0,0,1]
	v_cvt_pk_bf16_f32 v208, v196, v197
	v_cvt_pk_bf16_f32 v209, v198, v199
	v_cvt_pk_bf16_f32 v210, v200, v201
	v_cvt_pk_bf16_f32 v211, v202, v203
	global_store_dwordx4 v220, v[208:211], s[26:27]
	v_cndmask_b32_e64 v204, v32, v0, s[8:9]
	v_cndmask_b32_e64 v205, v33, v1, s[8:9]
	v_cndmask_b32_e64 v206, v34, v2, s[8:9]
	v_cndmask_b32_e64 v207, v35, v3, s[8:9]
	v_lshlrev_b32_e32 v196, 16, v204
	v_and_b32_e32 v197, 0xffff0000, v204
	v_lshlrev_b32_e32 v198, 16, v205
	v_and_b32_e32 v199, 0xffff0000, v205
	v_lshlrev_b32_e32 v200, 16, v206
	v_and_b32_e32 v201, 0xffff0000, v206
	v_lshlrev_b32_e32 v202, 16, v207
	v_and_b32_e32 v203, 0xffff0000, v207
	v_pk_add_f32 v[180:181], v[180:181], v[196:197] neg_lo:[0,1] neg_hi:[0,1]
	v_pk_add_f32 v[182:183], v[182:183], v[198:199] neg_lo:[0,1] neg_hi:[0,1]
	v_pk_add_f32 v[184:185], v[184:185], v[200:201] neg_lo:[0,1] neg_hi:[0,1]
	v_pk_add_f32 v[186:187], v[186:187], v[202:203] neg_lo:[0,1] neg_hi:[0,1]
	s_add_u32 s20, s24, 0x8000
	s_addc_u32 s21, s25, 0
	global_load_dwordx4 v[0:3], v221, s[20:21]
	global_load_dwordx4 v[32:35], v221, s[20:21] offset:2048
	s_add_i32 s2, s5, 2
	v_min_u32_e32 v217, s2, v219
	v_cvt_f32_u32_e32 v217, v217
	v_rcp_f32_e32 v216, v217
	s_waitcnt vmcnt(31)
	v_lshlrev_b32_e32 v188, 16, v64
	v_and_b32_e32 v189, 0xffff0000, v64
	v_lshlrev_b32_e32 v190, 16, v65
	v_and_b32_e32 v191, 0xffff0000, v65
	v_lshlrev_b32_e32 v192, 16, v66
	v_and_b32_e32 v193, 0xffff0000, v66
	v_lshlrev_b32_e32 v194, 16, v67
	v_and_b32_e32 v195, 0xffff0000, v67
	v_pk_add_f32 v[180:181], v[180:181], v[188:189]
	v_pk_add_f32 v[182:183], v[182:183], v[190:191]
	v_pk_add_f32 v[184:185], v[184:185], v[192:193]
	v_pk_add_f32 v[186:187], v[186:187], v[194:195]
	v_pk_fma_f32 v[196:197], v[180:181], v[216:217], v[188:189] op_sel_hi:[1,0,1] neg_lo:[0,0,1] neg_hi:[0,0,1]
	v_pk_fma_f32 v[198:199], v[182:183], v[216:217], v[190:191] op_sel_hi:[1,0,1] neg_lo:[0,0,1] neg_hi:[0,0,1]
	v_pk_fma_f32 v[200:201], v[184:185], v[216:217], v[192:193] op_sel_hi:[1,0,1] neg_lo:[0,0,1] neg_hi:[0,0,1]
	v_pk_fma_f32 v[202:203], v[186:187], v[216:217], v[194:195] op_sel_hi:[1,0,1] neg_lo:[0,0,1] neg_hi:[0,0,1]
	v_cvt_pk_bf16_f32 v212, v196, v197
	v_cvt_pk_bf16_f32 v213, v198, v199
	v_cvt_pk_bf16_f32 v214, v200, v201
	v_cvt_pk_bf16_f32 v215, v202, v203
	s_add_u32 s20, s26, 0x1000
	s_addc_u32 s21, s27, 0
	global_store_dwordx4 v220, v[212:215], s[20:21]
	v_cndmask_b32_e64 v204, v36, v4, s[8:9]
	v_cndmask_b32_e64 v205, v37, v5, s[8:9]
	v_cndmask_b32_e64 v206, v38, v6, s[8:9]
	v_cndmask_b32_e64 v207, v39, v7, s[8:9]
	v_lshlrev_b32_e32 v196, 16, v204
	v_and_b32_e32 v197, 0xffff0000, v204
	v_lshlrev_b32_e32 v198, 16, v205
	v_and_b32_e32 v199, 0xffff0000, v205
	v_lshlrev_b32_e32 v200, 16, v206
	v_and_b32_e32 v201, 0xffff0000, v206
	v_lshlrev_b32_e32 v202, 16, v207
	v_and_b32_e32 v203, 0xffff0000, v207
	v_pk_add_f32 v[180:181], v[180:181], v[196:197] neg_lo:[0,1] neg_hi:[0,1]
	v_pk_add_f32 v[182:183], v[182:183], v[198:199] neg_lo:[0,1] neg_hi:[0,1]
	v_pk_add_f32 v[184:185], v[184:185], v[200:201] neg_lo:[0,1] neg_hi:[0,1]
	v_pk_add_f32 v[186:187], v[186:187], v[202:203] neg_lo:[0,1] neg_hi:[0,1]
	s_add_u32 s20, s24, 0xc000
	s_addc_u32 s21, s25, 0
	global_load_dwordx4 v[4:7], v221, s[20:21]
	global_load_dwordx4 v[36:39], v221, s[20:21] offset:2048
	s_add_i32 s2, s5, 3
	v_min_u32_e32 v217, s2, v219
	v_cvt_f32_u32_e32 v217, v217
	v_rcp_f32_e32 v216, v217
	s_waitcnt vmcnt(33)
	v_lshlrev_b32_e32 v188, 16, v68
	v_and_b32_e32 v189, 0xffff0000, v68
	v_lshlrev_b32_e32 v190, 16, v69
	v_and_b32_e32 v191, 0xffff0000, v69
	v_lshlrev_b32_e32 v192, 16, v70
	v_and_b32_e32 v193, 0xffff0000, v70
	v_lshlrev_b32_e32 v194, 16, v71
	v_and_b32_e32 v195, 0xffff0000, v71
	v_pk_add_f32 v[180:181], v[180:181], v[188:189]
	v_pk_add_f32 v[182:183], v[182:183], v[190:191]
	v_pk_add_f32 v[184:185], v[184:185], v[192:193]
	v_pk_add_f32 v[186:187], v[186:187], v[194:195]
	v_pk_fma_f32 v[196:197], v[180:181], v[216:217], v[188:189] op_sel_hi:[1,0,1] neg_lo:[0,0,1] neg_hi:[0,0,1]
	v_pk_fma_f32 v[198:199], v[182:183], v[216:217], v[190:191] op_sel_hi:[1,0,1] neg_lo:[0,0,1] neg_hi:[0,0,1]
	v_pk_fma_f32 v[200:201], v[184:185], v[216:217], v[192:193] op_sel_hi:[1,0,1] neg_lo:[0,0,1] neg_hi:[0,0,1]
	v_pk_fma_f32 v[202:203], v[186:187], v[216:217], v[194:195] op_sel_hi:[1,0,1] neg_lo:[0,0,1] neg_hi:[0,0,1]
	v_cvt_pk_bf16_f32 v208, v196, v197
	v_cvt_pk_bf16_f32 v209, v198, v199
	v_cvt_pk_bf16_f32 v210, v200, v201
	v_cvt_pk_bf16_f32 v211, v202, v203
	s_add_u32 s20, s26, 0x2000
	s_addc_u32 s21, s27, 0
	global_store_dwordx4 v220, v[208:211], s[20:21]
	v_cndmask_b32_e64 v204, v40, v8, s[8:9]
	v_cndmask_b32_e64 v205, v41, v9, s[8:9]
	v_cndmask_b32_e64 v206, v42, v10, s[8:9]
	v_cndmask_b32_e64 v207, v43, v11, s[8:9]
	v_lshlrev_b32_e32 v196, 16, v204
	v_and_b32_e32 v197, 0xffff0000, v204
	v_lshlrev_b32_e32 v198, 16, v205
	v_and_b32_e32 v199, 0xffff0000, v205
	v_lshlrev_b32_e32 v200, 16, v206
	v_and_b32_e32 v201, 0xffff0000, v206
	v_lshlrev_b32_e32 v202, 16, v207
	v_and_b32_e32 v203, 0xffff0000, v207
	v_pk_add_f32 v[180:181], v[180:181], v[196:197] neg_lo:[0,1] neg_hi:[0,1]
	v_pk_add_f32 v[182:183], v[182:183], v[198:199] neg_lo:[0,1] neg_hi:[0,1]
	v_pk_add_f32 v[184:185], v[184:185], v[200:201] neg_lo:[0,1] neg_hi:[0,1]
	v_pk_add_f32 v[186:187], v[186:187], v[202:203] neg_lo:[0,1] neg_hi:[0,1]
	s_add_u32 s20, s24, 0x10000
	s_addc_u32 s21, s25, 0
	global_load_dwordx4 v[8:11], v221, s[20:21]
	global_load_dwordx4 v[40:43], v221, s[20:21] offset:2048
	s_add_i32 s2, s5, 4
	v_min_u32_e32 v217, s2, v219
	v_cvt_f32_u32_e32 v217, v217
	v_rcp_f32_e32 v216, v217
	s_waitcnt vmcnt(35)
	v_lshlrev_b32_e32 v188, 16, v72
	v_and_b32_e32 v189, 0xffff0000, v72
	v_lshlrev_b32_e32 v190, 16, v73
	v_and_b32_e32 v191, 0xffff0000, v73
	v_lshlrev_b32_e32 v192, 16, v74
	v_and_b32_e32 v193, 0xffff0000, v74
	v_lshlrev_b32_e32 v194, 16, v75
	v_and_b32_e32 v195, 0xffff0000, v75
	v_pk_add_f32 v[180:181], v[180:181], v[188:189]
	v_pk_add_f32 v[182:183], v[182:183], v[190:191]
	v_pk_add_f32 v[184:185], v[184:185], v[192:193]
	v_pk_add_f32 v[186:187], v[186:187], v[194:195]
	v_pk_fma_f32 v[196:197], v[180:181], v[216:217], v[188:189] op_sel_hi:[1,0,1] neg_lo:[0,0,1] neg_hi:[0,0,1]
	v_pk_fma_f32 v[198:199], v[182:183], v[216:217], v[190:191] op_sel_hi:[1,0,1] neg_lo:[0,0,1] neg_hi:[0,0,1]
	v_pk_fma_f32 v[200:201], v[184:185], v[216:217], v[192:193] op_sel_hi:[1,0,1] neg_lo:[0,0,1] neg_hi:[0,0,1]
	v_pk_fma_f32 v[202:203], v[186:187], v[216:217], v[194:195] op_sel_hi:[1,0,1] neg_lo:[0,0,1] neg_hi:[0,0,1]
	v_cvt_pk_bf16_f32 v212, v196, v197
	v_cvt_pk_bf16_f32 v213, v198, v199
	v_cvt_pk_bf16_f32 v214, v200, v201
	v_cvt_pk_bf16_f32 v215, v202, v203
	s_add_u32 s20, s26, 0x3000
	s_addc_u32 s21, s27, 0
	global_store_dwordx4 v220, v[212:215], s[20:21]
	v_cndmask_b32_e64 v204, v44, v12, s[8:9]
	v_cndmask_b32_e64 v205, v45, v13, s[8:9]
	v_cndmask_b32_e64 v206, v46, v14, s[8:9]
	v_cndmask_b32_e64 v207, v47, v15, s[8:9]
	v_lshlrev_b32_e32 v196, 16, v204
	v_and_b32_e32 v197, 0xffff0000, v204
	v_lshlrev_b32_e32 v198, 16, v205
	v_and_b32_e32 v199, 0xffff0000, v205
	v_lshlrev_b32_e32 v200, 16, v206
	v_and_b32_e32 v201, 0xffff0000, v206
	v_lshlrev_b32_e32 v202, 16, v207
	v_and_b32_e32 v203, 0xffff0000, v207
	v_pk_add_f32 v[180:181], v[180:181], v[196:197] neg_lo:[0,1] neg_hi:[0,1]
	v_pk_add_f32 v[182:183], v[182:183], v[198:199] neg_lo:[0,1] neg_hi:[0,1]
	v_pk_add_f32 v[184:185], v[184:185], v[200:201] neg_lo:[0,1] neg_hi:[0,1]
	v_pk_add_f32 v[186:187], v[186:187], v[202:203] neg_lo:[0,1] neg_hi:[0,1]
	s_add_u32 s20, s24, 0x14000
	s_addc_u32 s21, s25, 0
	global_load_dwordx4 v[12:15], v221, s[20:21]
	global_load_dwordx4 v[44:47], v221, s[20:21] offset:2048
	s_add_i32 s2, s5, 5
	v_min_u32_e32 v217, s2, v219
	v_cvt_f32_u32_e32 v217, v217
	v_rcp_f32_e32 v216, v217
	s_waitcnt vmcnt(37)
	v_lshlrev_b32_e32 v188, 16, v76
	v_and_b32_e32 v189, 0xffff0000, v76
	v_lshlrev_b32_e32 v190, 16, v77
	v_and_b32_e32 v191, 0xffff0000, v77
	v_lshlrev_b32_e32 v192, 16, v78
	v_and_b32_e32 v193, 0xffff0000, v78
	v_lshlrev_b32_e32 v194, 16, v79
	v_and_b32_e32 v195, 0xffff0000, v79
	v_pk_add_f32 v[180:181], v[180:181], v[188:189]
	v_pk_add_f32 v[182:183], v[182:183], v[190:191]
	v_pk_add_f32 v[184:185], v[184:185], v[192:193]
	v_pk_add_f32 v[186:187], v[186:187], v[194:195]
	v_pk_fma_f32 v[196:197], v[180:181], v[216:217], v[188:189] op_sel_hi:[1,0,1] neg_lo:[0,0,1] neg_hi:[0,0,1]
	v_pk_fma_f32 v[198:199], v[182:183], v[216:217], v[190:191] op_sel_hi:[1,0,1] neg_lo:[0,0,1] neg_hi:[0,0,1]
	v_pk_fma_f32 v[200:201], v[184:185], v[216:217], v[192:193] op_sel_hi:[1,0,1] neg_lo:[0,0,1] neg_hi:[0,0,1]
	v_pk_fma_f32 v[202:203], v[186:187], v[216:217], v[194:195] op_sel_hi:[1,0,1] neg_lo:[0,0,1] neg_hi:[0,0,1]
	v_cvt_pk_bf16_f32 v208, v196, v197
	v_cvt_pk_bf16_f32 v209, v198, v199
	v_cvt_pk_bf16_f32 v210, v200, v201
	v_cvt_pk_bf16_f32 v211, v202, v203
	s_add_u32 s20, s26, 0x4000
	s_addc_u32 s21, s27, 0
	global_store_dwordx4 v220, v[208:211], s[20:21]
	v_cndmask_b32_e64 v204, v48, v16, s[8:9]
	v_cndmask_b32_e64 v205, v49, v17, s[8:9]
	v_cndmask_b32_e64 v206, v50, v18, s[8:9]
	v_cndmask_b32_e64 v207, v51, v19, s[8:9]
	v_lshlrev_b32_e32 v196, 16, v204
	v_and_b32_e32 v197, 0xffff0000, v204
	v_lshlrev_b32_e32 v198, 16, v205
	v_and_b32_e32 v199, 0xffff0000, v205
	v_lshlrev_b32_e32 v200, 16, v206
	v_and_b32_e32 v201, 0xffff0000, v206
	v_lshlrev_b32_e32 v202, 16, v207
	v_and_b32_e32 v203, 0xffff0000, v207
	v_pk_add_f32 v[180:181], v[180:181], v[196:197] neg_lo:[0,1] neg_hi:[0,1]
	v_pk_add_f32 v[182:183], v[182:183], v[198:199] neg_lo:[0,1] neg_hi:[0,1]
	v_pk_add_f32 v[184:185], v[184:185], v[200:201] neg_lo:[0,1] neg_hi:[0,1]
	v_pk_add_f32 v[186:187], v[186:187], v[202:203] neg_lo:[0,1] neg_hi:[0,1]
	s_add_u32 s20, s24, 0x18000
	s_addc_u32 s21, s25, 0
	global_load_dwordx4 v[16:19], v221, s[20:21]
	global_load_dwordx4 v[48:51], v221, s[20:21] offset:2048
	s_add_i32 s2, s5, 6
	v_min_u32_e32 v217, s2, v219
	v_cvt_f32_u32_e32 v217, v217
	v_rcp_f32_e32 v216, v217
	s_waitcnt vmcnt(39)
	v_lshlrev_b32_e32 v188, 16, v80
	v_and_b32_e32 v189, 0xffff0000, v80
	v_lshlrev_b32_e32 v190, 16, v81
	v_and_b32_e32 v191, 0xffff0000, v81
	v_lshlrev_b32_e32 v192, 16, v82
	v_and_b32_e32 v193, 0xffff0000, v82
	v_lshlrev_b32_e32 v194, 16, v83
	v_and_b32_e32 v195, 0xffff0000, v83
	v_pk_add_f32 v[180:181], v[180:181], v[188:189]
	v_pk_add_f32 v[182:183], v[182:183], v[190:191]
	v_pk_add_f32 v[184:185], v[184:185], v[192:193]
	v_pk_add_f32 v[186:187], v[186:187], v[194:195]
	v_pk_fma_f32 v[196:197], v[180:181], v[216:217], v[188:189] op_sel_hi:[1,0,1] neg_lo:[0,0,1] neg_hi:[0,0,1]
	v_pk_fma_f32 v[198:199], v[182:183], v[216:217], v[190:191] op_sel_hi:[1,0,1] neg_lo:[0,0,1] neg_hi:[0,0,1]
	v_pk_fma_f32 v[200:201], v[184:185], v[216:217], v[192:193] op_sel_hi:[1,0,1] neg_lo:[0,0,1] neg_hi:[0,0,1]
	v_pk_fma_f32 v[202:203], v[186:187], v[216:217], v[194:195] op_sel_hi:[1,0,1] neg_lo:[0,0,1] neg_hi:[0,0,1]
	v_cvt_pk_bf16_f32 v212, v196, v197
	v_cvt_pk_bf16_f32 v213, v198, v199
	v_cvt_pk_bf16_f32 v214, v200, v201
	v_cvt_pk_bf16_f32 v215, v202, v203
	s_add_u32 s20, s26, 0x5000
	s_addc_u32 s21, s27, 0
	global_store_dwordx4 v220, v[212:215], s[20:21]
	v_cndmask_b32_e64 v204, v52, v20, s[8:9]
	v_cndmask_b32_e64 v205, v53, v21, s[8:9]
	v_cndmask_b32_e64 v206, v54, v22, s[8:9]
	v_cndmask_b32_e64 v207, v55, v23, s[8:9]
	v_lshlrev_b32_e32 v196, 16, v204
	v_and_b32_e32 v197, 0xffff0000, v204
	v_lshlrev_b32_e32 v198, 16, v205
	v_and_b32_e32 v199, 0xffff0000, v205
	v_lshlrev_b32_e32 v200, 16, v206
	v_and_b32_e32 v201, 0xffff0000, v206
	v_lshlrev_b32_e32 v202, 16, v207
	v_and_b32_e32 v203, 0xffff0000, v207
	v_pk_add_f32 v[180:181], v[180:181], v[196:197] neg_lo:[0,1] neg_hi:[0,1]
	v_pk_add_f32 v[182:183], v[182:183], v[198:199] neg_lo:[0,1] neg_hi:[0,1]
	v_pk_add_f32 v[184:185], v[184:185], v[200:201] neg_lo:[0,1] neg_hi:[0,1]
	v_pk_add_f32 v[186:187], v[186:187], v[202:203] neg_lo:[0,1] neg_hi:[0,1]
	s_add_u32 s20, s24, 0x1c000
	s_addc_u32 s21, s25, 0
	global_load_dwordx4 v[20:23], v221, s[20:21]
	global_load_dwordx4 v[52:55], v221, s[20:21] offset:2048
	s_add_i32 s2, s5, 7
	v_min_u32_e32 v217, s2, v219
	v_cvt_f32_u32_e32 v217, v217
	v_rcp_f32_e32 v216, v217
	s_waitcnt vmcnt(41)
	v_lshlrev_b32_e32 v188, 16, v84
	v_and_b32_e32 v189, 0xffff0000, v84
	v_lshlrev_b32_e32 v190, 16, v85
	v_and_b32_e32 v191, 0xffff0000, v85
	v_lshlrev_b32_e32 v192, 16, v86
	v_and_b32_e32 v193, 0xffff0000, v86
	v_lshlrev_b32_e32 v194, 16, v87
	v_and_b32_e32 v195, 0xffff0000, v87
	v_pk_add_f32 v[180:181], v[180:181], v[188:189]
	v_pk_add_f32 v[182:183], v[182:183], v[190:191]
	v_pk_add_f32 v[184:185], v[184:185], v[192:193]
	v_pk_add_f32 v[186:187], v[186:187], v[194:195]
	v_pk_fma_f32 v[196:197], v[180:181], v[216:217], v[188:189] op_sel_hi:[1,0,1] neg_lo:[0,0,1] neg_hi:[0,0,1]
	v_pk_fma_f32 v[198:199], v[182:183], v[216:217], v[190:191] op_sel_hi:[1,0,1] neg_lo:[0,0,1] neg_hi:[0,0,1]
	v_pk_fma_f32 v[200:201], v[184:185], v[216:217], v[192:193] op_sel_hi:[1,0,1] neg_lo:[0,0,1] neg_hi:[0,0,1]
	v_pk_fma_f32 v[202:203], v[186:187], v[216:217], v[194:195] op_sel_hi:[1,0,1] neg_lo:[0,0,1] neg_hi:[0,0,1]
	v_cvt_pk_bf16_f32 v208, v196, v197
	v_cvt_pk_bf16_f32 v209, v198, v199
	v_cvt_pk_bf16_f32 v210, v200, v201
	v_cvt_pk_bf16_f32 v211, v202, v203
	s_add_u32 s20, s26, 0x6000
	s_addc_u32 s21, s27, 0
	global_store_dwordx4 v220, v[208:211], s[20:21]
	v_cndmask_b32_e64 v204, v56, v24, s[8:9]
	v_cndmask_b32_e64 v205, v57, v25, s[8:9]
	v_cndmask_b32_e64 v206, v58, v26, s[8:9]
	v_cndmask_b32_e64 v207, v59, v27, s[8:9]
	v_lshlrev_b32_e32 v196, 16, v204
	v_and_b32_e32 v197, 0xffff0000, v204
	v_lshlrev_b32_e32 v198, 16, v205
	v_and_b32_e32 v199, 0xffff0000, v205
	v_lshlrev_b32_e32 v200, 16, v206
	v_and_b32_e32 v201, 0xffff0000, v206
	v_lshlrev_b32_e32 v202, 16, v207
	v_and_b32_e32 v203, 0xffff0000, v207
	v_pk_add_f32 v[180:181], v[180:181], v[196:197] neg_lo:[0,1] neg_hi:[0,1]
	v_pk_add_f32 v[182:183], v[182:183], v[198:199] neg_lo:[0,1] neg_hi:[0,1]
	v_pk_add_f32 v[184:185], v[184:185], v[200:201] neg_lo:[0,1] neg_hi:[0,1]
	v_pk_add_f32 v[186:187], v[186:187], v[202:203] neg_lo:[0,1] neg_hi:[0,1]
	s_add_i32 s2, s5, 8
	v_min_u32_e32 v217, s2, v219
	v_cvt_f32_u32_e32 v217, v217
	v_rcp_f32_e32 v216, v217
	s_waitcnt vmcnt(41)
	v_lshlrev_b32_e32 v188, 16, v88
	v_and_b32_e32 v189, 0xffff0000, v88
	v_lshlrev_b32_e32 v190, 16, v89
	v_and_b32_e32 v191, 0xffff0000, v89
	v_lshlrev_b32_e32 v192, 16, v90
	v_and_b32_e32 v193, 0xffff0000, v90
	v_lshlrev_b32_e32 v194, 16, v91
	v_and_b32_e32 v195, 0xffff0000, v91
	v_pk_add_f32 v[180:181], v[180:181], v[188:189]
	v_pk_add_f32 v[182:183], v[182:183], v[190:191]
	v_pk_add_f32 v[184:185], v[184:185], v[192:193]
	v_pk_add_f32 v[186:187], v[186:187], v[194:195]
	v_pk_fma_f32 v[196:197], v[180:181], v[216:217], v[188:189] op_sel_hi:[1,0,1] neg_lo:[0,0,1] neg_hi:[0,0,1]
	v_pk_fma_f32 v[198:199], v[182:183], v[216:217], v[190:191] op_sel_hi:[1,0,1] neg_lo:[0,0,1] neg_hi:[0,0,1]
	v_pk_fma_f32 v[200:201], v[184:185], v[216:217], v[192:193] op_sel_hi:[1,0,1] neg_lo:[0,0,1] neg_hi:[0,0,1]
	v_pk_fma_f32 v[202:203], v[186:187], v[216:217], v[194:195] op_sel_hi:[1,0,1] neg_lo:[0,0,1] neg_hi:[0,0,1]
	v_cvt_pk_bf16_f32 v212, v196, v197
	v_cvt_pk_bf16_f32 v213, v198, v199
	v_cvt_pk_bf16_f32 v214, v200, v201
	v_cvt_pk_bf16_f32 v215, v202, v203
	s_add_u32 s20, s26, 0x7000
	s_addc_u32 s21, s27, 0
	global_store_dwordx4 v220, v[212:215], s[20:21]
	s_waitcnt vmcnt(26)
	s_add_i32 s2, s5, -2
	s_cmp_lt_i32 s2, 0
	s_cselect_b32 s2, 0, -1
	v_and_b32_e32 v148, s2, v148
	v_and_b32_e32 v149, s2, v149
	v_and_b32_e32 v150, s2, v150
	v_and_b32_e32 v151, s2, v151
	v_lshlrev_b32_e32 v180, 16, v148
	v_and_b32_e32 v181, 0xffff0000, v148
	v_lshlrev_b32_e32 v182, 16, v149
	v_and_b32_e32 v183, 0xffff0000, v149
	v_lshlrev_b32_e32 v184, 16, v150
	v_and_b32_e32 v185, 0xffff0000, v150
	v_lshlrev_b32_e32 v186, 16, v151
	v_and_b32_e32 v187, 0xffff0000, v151
	v_lshlrev_b32_e32 v188, 16, v152
	v_and_b32_e32 v189, 0xffff0000, v152
	v_lshlrev_b32_e32 v190, 16, v153
	v_and_b32_e32 v191, 0xffff0000, v153
	v_lshlrev_b32_e32 v192, 16, v154
	v_and_b32_e32 v193, 0xffff0000, v154
	v_lshlrev_b32_e32 v194, 16, v155
	v_and_b32_e32 v195, 0xffff0000, v155
	v_pk_mul_f32 v[56:57], v[180:181], v[188:189]
	v_pk_mul_f32 v[58:59], v[182:183], v[190:191]
	v_pk_mul_f32 v[60:61], v[184:185], v[192:193]
	v_pk_mul_f32 v[62:63], v[186:187], v[194:195]
	s_waitcnt vmcnt(24)
	s_add_i32 s2, s5, -1
	s_cmp_lt_i32 s2, 0
	s_cselect_b32 s2, 0, -1
	v_and_b32_e32 v156, s2, v156
	v_and_b32_e32 v157, s2, v157
	v_and_b32_e32 v158, s2, v158
	v_and_b32_e32 v159, s2, v159
	v_lshlrev_b32_e32 v180, 16, v156
	v_and_b32_e32 v181, 0xffff0000, v156
	v_lshlrev_b32_e32 v182, 16, v157
	v_and_b32_e32 v183, 0xffff0000, v157
	v_lshlrev_b32_e32 v184, 16, v158
	v_and_b32_e32 v185, 0xffff0000, v158
	v_lshlrev_b32_e32 v186, 16, v159
	v_and_b32_e32 v187, 0xffff0000, v159
	v_lshlrev_b32_e32 v188, 16, v160
	v_and_b32_e32 v189, 0xffff0000, v160
	v_lshlrev_b32_e32 v190, 16, v161
	v_and_b32_e32 v191, 0xffff0000, v161
	v_lshlrev_b32_e32 v192, 16, v162
	v_and_b32_e32 v193, 0xffff0000, v162
	v_lshlrev_b32_e32 v194, 16, v163
	v_and_b32_e32 v195, 0xffff0000, v163
	v_pk_mul_f32 v[64:65], v[180:181], v[188:189]
	v_pk_mul_f32 v[66:67], v[182:183], v[190:191]
	v_pk_mul_f32 v[68:69], v[184:185], v[192:193]
	v_pk_mul_f32 v[70:71], v[186:187], v[194:195]
	s_waitcnt vmcnt(22)
	v_lshlrev_b32_e32 v180, 16, v164
	v_and_b32_e32 v181, 0xffff0000, v164
	v_lshlrev_b32_e32 v182, 16, v165
	v_and_b32_e32 v183, 0xffff0000, v165
	v_lshlrev_b32_e32 v184, 16, v166
	v_and_b32_e32 v185, 0xffff0000, v166
	v_lshlrev_b32_e32 v186, 16, v167
	v_and_b32_e32 v187, 0xffff0000, v167
	v_lshlrev_b32_e32 v188, 16, v168
	v_and_b32_e32 v189, 0xffff0000, v168
	v_lshlrev_b32_e32 v190, 16, v169
	v_and_b32_e32 v191, 0xffff0000, v169
	v_lshlrev_b32_e32 v192, 16, v170
	v_and_b32_e32 v193, 0xffff0000, v170
	v_lshlrev_b32_e32 v194, 16, v171
	v_and_b32_e32 v195, 0xffff0000, v171
	v_pk_mul_f32 v[72:73], v[180:181], v[188:189]
	v_pk_mul_f32 v[74:75], v[182:183], v[190:191]
	v_pk_mul_f32 v[76:77], v[184:185], v[192:193]
	v_pk_mul_f32 v[78:79], v[186:187], v[194:195]
	v_pk_mul_f32 v[80:81], v[92:93], v[56:57]
	v_pk_mul_f32 v[82:83], v[94:95], v[58:59]
	v_pk_mul_f32 v[84:85], v[96:97], v[60:61]
	v_pk_mul_f32 v[86:87], v[98:99], v[62:63]
	v_pk_fma_f32 v[80:81], v[100:101], v[64:65], v[80:81]
	v_pk_fma_f32 v[82:83], v[102:103], v[66:67], v[82:83]
	v_pk_fma_f32 v[84:85], v[104:105], v[68:69], v[84:85]
	v_pk_fma_f32 v[86:87], v[106:107], v[70:71], v[86:87]
	v_pk_fma_f32 v[80:81], v[108:109], v[72:73], v[80:81]
	v_pk_fma_f32 v[82:83], v[110:111], v[74:75], v[82:83]
	v_pk_fma_f32 v[84:85], v[112:113], v[76:77], v[84:85]
	v_pk_fma_f32 v[86:87], v[114:115], v[78:79], v[86:87]
	s_waitcnt vmcnt(35)
	v_lshlrev_b32_e32 v196, 16, v116
	v_and_b32_e32 v197, 0xffff0000, v116
	v_lshlrev_b32_e32 v198, 16, v117
	v_and_b32_e32 v199, 0xffff0000, v117
	v_lshlrev_b32_e32 v200, 16, v118
	v_and_b32_e32 v201, 0xffff0000, v118
	v_lshlrev_b32_e32 v202, 16, v119
	v_and_b32_e32 v203, 0xffff0000, v119
	v_pk_mul_f32 v[80:81], v[80:81], v[196:197]
	v_pk_mul_f32 v[82:83], v[82:83], v[198:199]
	v_pk_mul_f32 v[84:85], v[84:85], v[200:201]
	v_pk_mul_f32 v[86:87], v[86:87], v[202:203]
	v_cvt_pk_bf16_f32 v208, v80, v81
	v_cvt_pk_bf16_f32 v209, v82, v83
	v_cvt_pk_bf16_f32 v210, v84, v85
	v_cvt_pk_bf16_f32 v211, v86, v87
	global_store_dwordx4 v220, v[208:211], s[26:27] offset:2048
	s_waitcnt vmcnt(21)
	v_lshlrev_b32_e32 v180, 16, v172
	v_and_b32_e32 v181, 0xffff0000, v172
	v_lshlrev_b32_e32 v182, 16, v173
	v_and_b32_e32 v183, 0xffff0000, v173
	v_lshlrev_b32_e32 v184, 16, v174
	v_and_b32_e32 v185, 0xffff0000, v174
	v_lshlrev_b32_e32 v186, 16, v175
	v_and_b32_e32 v187, 0xffff0000, v175
	v_lshlrev_b32_e32 v188, 16, v176
	v_and_b32_e32 v189, 0xffff0000, v176
	v_lshlrev_b32_e32 v190, 16, v177
	v_and_b32_e32 v191, 0xffff0000, v177
	v_lshlrev_b32_e32 v192, 16, v178
	v_and_b32_e32 v193, 0xffff0000, v178
	v_lshlrev_b32_e32 v194, 16, v179
	v_and_b32_e32 v195, 0xffff0000, v179
	v_pk_mul_f32 v[56:57], v[180:181], v[188:189]
	v_pk_mul_f32 v[58:59], v[182:183], v[190:191]
	v_pk_mul_f32 v[60:61], v[184:185], v[192:193]
	v_pk_mul_f32 v[62:63], v[186:187], v[194:195]
	v_pk_mul_f32 v[80:81], v[92:93], v[64:65]
	v_pk_mul_f32 v[82:83], v[94:95], v[66:67]
	v_pk_mul_f32 v[84:85], v[96:97], v[68:69]
	v_pk_mul_f32 v[86:87], v[98:99], v[70:71]
	v_pk_fma_f32 v[80:81], v[100:101], v[72:73], v[80:81]
	v_pk_fma_f32 v[82:83], v[102:103], v[74:75], v[82:83]
	v_pk_fma_f32 v[84:85], v[104:105], v[76:77], v[84:85]
	v_pk_fma_f32 v[86:87], v[106:107], v[78:79], v[86:87]
	v_pk_fma_f32 v[80:81], v[108:109], v[56:57], v[80:81]
	v_pk_fma_f32 v[82:83], v[110:111], v[58:59], v[82:83]
	v_pk_fma_f32 v[84:85], v[112:113], v[60:61], v[84:85]
	v_pk_fma_f32 v[86:87], v[114:115], v[62:63], v[86:87]
	s_waitcnt vmcnt(35)
	v_lshlrev_b32_e32 v196, 16, v120
	v_and_b32_e32 v197, 0xffff0000, v120
	v_lshlrev_b32_e32 v198, 16, v121
	v_and_b32_e32 v199, 0xffff0000, v121
	v_lshlrev_b32_e32 v200, 16, v122
	v_and_b32_e32 v201, 0xffff0000, v122
	v_lshlrev_b32_e32 v202, 16, v123
	v_and_b32_e32 v203, 0xffff0000, v123
	v_pk_mul_f32 v[80:81], v[80:81], v[196:197]
	v_pk_mul_f32 v[82:83], v[82:83], v[198:199]
	v_pk_mul_f32 v[84:85], v[84:85], v[200:201]
	v_pk_mul_f32 v[86:87], v[86:87], v[202:203]
	v_cvt_pk_bf16_f32 v212, v80, v81
	v_cvt_pk_bf16_f32 v213, v82, v83
	v_cvt_pk_bf16_f32 v214, v84, v85
	v_cvt_pk_bf16_f32 v215, v86, v87
	s_add_u32 s20, s26, 0x1000
	s_addc_u32 s21, s27, 0
	global_store_dwordx4 v220, v[212:215], s[20:21] offset:2048
	s_waitcnt vmcnt(19)
	v_lshlrev_b32_e32 v180, 16, v0
	v_and_b32_e32 v181, 0xffff0000, v0
	v_lshlrev_b32_e32 v182, 16, v1
	v_and_b32_e32 v183, 0xffff0000, v1
	v_lshlrev_b32_e32 v184, 16, v2
	v_and_b32_e32 v185, 0xffff0000, v2
	v_lshlrev_b32_e32 v186, 16, v3
	v_and_b32_e32 v187, 0xffff0000, v3
	v_lshlrev_b32_e32 v188, 16, v32
	v_and_b32_e32 v189, 0xffff0000, v32
	v_lshlrev_b32_e32 v190, 16, v33
	v_and_b32_e32 v191, 0xffff0000, v33
	v_lshlrev_b32_e32 v192, 16, v34
	v_and_b32_e32 v193, 0xffff0000, v34
	v_lshlrev_b32_e32 v194, 16, v35
	v_and_b32_e32 v195, 0xffff0000, v35
	v_pk_mul_f32 v[64:65], v[180:181], v[188:189]
	v_pk_mul_f32 v[66:67], v[182:183], v[190:191]
	v_pk_mul_f32 v[68:69], v[184:185], v[192:193]
	v_pk_mul_f32 v[70:71], v[186:187], v[194:195]
	v_pk_mul_f32 v[80:81], v[92:93], v[72:73]
	v_pk_mul_f32 v[82:83], v[94:95], v[74:75]
	v_pk_mul_f32 v[84:85], v[96:97], v[76:77]
	v_pk_mul_f32 v[86:87], v[98:99], v[78:79]
	v_pk_fma_f32 v[80:81], v[100:101], v[56:57], v[80:81]
	v_pk_fma_f32 v[82:83], v[102:103], v[58:59], v[82:83]
	v_pk_fma_f32 v[84:85], v[104:105], v[60:61], v[84:85]
	v_pk_fma_f32 v[86:87], v[106:107], v[62:63], v[86:87]
	v_pk_fma_f32 v[80:81], v[108:109], v[64:65], v[80:81]
	v_pk_fma_f32 v[82:83], v[110:111], v[66:67], v[82:83]
	v_pk_fma_f32 v[84:85], v[112:113], v[68:69], v[84:85]
	v_pk_fma_f32 v[86:87], v[114:115], v[70:71], v[86:87]
	s_waitcnt vmcnt(35)
	v_lshlrev_b32_e32 v196, 16, v124
	v_and_b32_e32 v197, 0xffff0000, v124
	v_lshlrev_b32_e32 v198, 16, v125
	v_and_b32_e32 v199, 0xffff0000, v125
	v_lshlrev_b32_e32 v200, 16, v126
	v_and_b32_e32 v201, 0xffff0000, v126
	v_lshlrev_b32_e32 v202, 16, v127
	v_and_b32_e32 v203, 0xffff0000, v127
	v_pk_mul_f32 v[80:81], v[80:81], v[196:197]
	v_pk_mul_f32 v[82:83], v[82:83], v[198:199]
	v_pk_mul_f32 v[84:85], v[84:85], v[200:201]
	v_pk_mul_f32 v[86:87], v[86:87], v[202:203]
	v_cvt_pk_bf16_f32 v208, v80, v81
	v_cvt_pk_bf16_f32 v209, v82, v83
	v_cvt_pk_bf16_f32 v210, v84, v85
	v_cvt_pk_bf16_f32 v211, v86, v87
	s_add_u32 s20, s26, 0x2000
	s_addc_u32 s21, s27, 0
	global_store_dwordx4 v220, v[208:211], s[20:21] offset:2048
	s_waitcnt vmcnt(17)
	v_lshlrev_b32_e32 v180, 16, v4
	v_and_b32_e32 v181, 0xffff0000, v4
	v_lshlrev_b32_e32 v182, 16, v5
	v_and_b32_e32 v183, 0xffff0000, v5
	v_lshlrev_b32_e32 v184, 16, v6
	v_and_b32_e32 v185, 0xffff0000, v6
	v_lshlrev_b32_e32 v186, 16, v7
	v_and_b32_e32 v187, 0xffff0000, v7
	v_lshlrev_b32_e32 v188, 16, v36
	v_and_b32_e32 v189, 0xffff0000, v36
	v_lshlrev_b32_e32 v190, 16, v37
	v_and_b32_e32 v191, 0xffff0000, v37
	v_lshlrev_b32_e32 v192, 16, v38
	v_and_b32_e32 v193, 0xffff0000, v38
	v_lshlrev_b32_e32 v194, 16, v39
	v_and_b32_e32 v195, 0xffff0000, v39
	v_pk_mul_f32 v[72:73], v[180:181], v[188:189]
	v_pk_mul_f32 v[74:75], v[182:183], v[190:191]
	v_pk_mul_f32 v[76:77], v[184:185], v[192:193]
	v_pk_mul_f32 v[78:79], v[186:187], v[194:195]
	v_pk_mul_f32 v[80:81], v[92:93], v[56:57]
	v_pk_mul_f32 v[82:83], v[94:95], v[58:59]
	v_pk_mul_f32 v[84:85], v[96:97], v[60:61]
	v_pk_mul_f32 v[86:87], v[98:99], v[62:63]
	v_pk_fma_f32 v[80:81], v[100:101], v[64:65], v[80:81]
	v_pk_fma_f32 v[82:83], v[102:103], v[66:67], v[82:83]
	v_pk_fma_f32 v[84:85], v[104:105], v[68:69], v[84:85]
	v_pk_fma_f32 v[86:87], v[106:107], v[70:71], v[86:87]
	v_pk_fma_f32 v[80:81], v[108:109], v[72:73], v[80:81]
	v_pk_fma_f32 v[82:83], v[110:111], v[74:75], v[82:83]
	v_pk_fma_f32 v[84:85], v[112:113], v[76:77], v[84:85]
	v_pk_fma_f32 v[86:87], v[114:115], v[78:79], v[86:87]
	s_waitcnt vmcnt(35)
	v_lshlrev_b32_e32 v196, 16, v128
	v_and_b32_e32 v197, 0xffff0000, v128
	v_lshlrev_b32_e32 v198, 16, v129
	v_and_b32_e32 v199, 0xffff0000, v129
	v_lshlrev_b32_e32 v200, 16, v130
	v_and_b32_e32 v201, 0xffff0000, v130
	v_lshlrev_b32_e32 v202, 16, v131
	v_and_b32_e32 v203, 0xffff0000, v131
	v_pk_mul_f32 v[80:81], v[80:81], v[196:197]
	v_pk_mul_f32 v[82:83], v[82:83], v[198:199]
	v_pk_mul_f32 v[84:85], v[84:85], v[200:201]
	v_pk_mul_f32 v[86:87], v[86:87], v[202:203]
	v_cvt_pk_bf16_f32 v212, v80, v81
	v_cvt_pk_bf16_f32 v213, v82, v83
	v_cvt_pk_bf16_f32 v214, v84, v85
	v_cvt_pk_bf16_f32 v215, v86, v87
	s_add_u32 s20, s26, 0x3000
	s_addc_u32 s21, s27, 0
	global_store_dwordx4 v220, v[212:215], s[20:21] offset:2048
	s_waitcnt vmcnt(15)
	v_lshlrev_b32_e32 v180, 16, v8
	v_and_b32_e32 v181, 0xffff0000, v8
	v_lshlrev_b32_e32 v182, 16, v9
	v_and_b32_e32 v183, 0xffff0000, v9
	v_lshlrev_b32_e32 v184, 16, v10
	v_and_b32_e32 v185, 0xffff0000, v10
	v_lshlrev_b32_e32 v186, 16, v11
	v_and_b32_e32 v187, 0xffff0000, v11
	v_lshlrev_b32_e32 v188, 16, v40
	v_and_b32_e32 v189, 0xffff0000, v40
	v_lshlrev_b32_e32 v190, 16, v41
	v_and_b32_e32 v191, 0xffff0000, v41
	v_lshlrev_b32_e32 v192, 16, v42
	v_and_b32_e32 v193, 0xffff0000, v42
	v_lshlrev_b32_e32 v194, 16, v43
	v_and_b32_e32 v195, 0xffff0000, v43
	v_pk_mul_f32 v[56:57], v[180:181], v[188:189]
	v_pk_mul_f32 v[58:59], v[182:183], v[190:191]
	v_pk_mul_f32 v[60:61], v[184:185], v[192:193]
	v_pk_mul_f32 v[62:63], v[186:187], v[194:195]
	v_pk_mul_f32 v[80:81], v[92:93], v[64:65]
	v_pk_mul_f32 v[82:83], v[94:95], v[66:67]
	v_pk_mul_f32 v[84:85], v[96:97], v[68:69]
	v_pk_mul_f32 v[86:87], v[98:99], v[70:71]
	v_pk_fma_f32 v[80:81], v[100:101], v[72:73], v[80:81]
	v_pk_fma_f32 v[82:83], v[102:103], v[74:75], v[82:83]
	v_pk_fma_f32 v[84:85], v[104:105], v[76:77], v[84:85]
	v_pk_fma_f32 v[86:87], v[106:107], v[78:79], v[86:87]
	v_pk_fma_f32 v[80:81], v[108:109], v[56:57], v[80:81]
	v_pk_fma_f32 v[82:83], v[110:111], v[58:59], v[82:83]
	v_pk_fma_f32 v[84:85], v[112:113], v[60:61], v[84:85]
	v_pk_fma_f32 v[86:87], v[114:115], v[62:63], v[86:87]
	s_waitcnt vmcnt(35)
	v_lshlrev_b32_e32 v196, 16, v132
	v_and_b32_e32 v197, 0xffff0000, v132
	v_lshlrev_b32_e32 v198, 16, v133
	v_and_b32_e32 v199, 0xffff0000, v133
	v_lshlrev_b32_e32 v200, 16, v134
	v_and_b32_e32 v201, 0xffff0000, v134
	v_lshlrev_b32_e32 v202, 16, v135
	v_and_b32_e32 v203, 0xffff0000, v135
	v_pk_mul_f32 v[80:81], v[80:81], v[196:197]
	v_pk_mul_f32 v[82:83], v[82:83], v[198:199]
	v_pk_mul_f32 v[84:85], v[84:85], v[200:201]
	v_pk_mul_f32 v[86:87], v[86:87], v[202:203]
	v_cvt_pk_bf16_f32 v208, v80, v81
	v_cvt_pk_bf16_f32 v209, v82, v83
	v_cvt_pk_bf16_f32 v210, v84, v85
	v_cvt_pk_bf16_f32 v211, v86, v87
	s_add_u32 s20, s26, 0x4000
	s_addc_u32 s21, s27, 0
	global_store_dwordx4 v220, v[208:211], s[20:21] offset:2048
	s_waitcnt vmcnt(13)
	v_lshlrev_b32_e32 v180, 16, v12
	v_and_b32_e32 v181, 0xffff0000, v12
	v_lshlrev_b32_e32 v182, 16, v13
	v_and_b32_e32 v183, 0xffff0000, v13
	v_lshlrev_b32_e32 v184, 16, v14
	v_and_b32_e32 v185, 0xffff0000, v14
	v_lshlrev_b32_e32 v186, 16, v15
	v_and_b32_e32 v187, 0xffff0000, v15
	v_lshlrev_b32_e32 v188, 16, v44
	v_and_b32_e32 v189, 0xffff0000, v44
	v_lshlrev_b32_e32 v190, 16, v45
	v_and_b32_e32 v191, 0xffff0000, v45
	v_lshlrev_b32_e32 v192, 16, v46
	v_and_b32_e32 v193, 0xffff0000, v46
	v_lshlrev_b32_e32 v194, 16, v47
	v_and_b32_e32 v195, 0xffff0000, v47
	v_pk_mul_f32 v[64:65], v[180:181], v[188:189]
	v_pk_mul_f32 v[66:67], v[182:183], v[190:191]
	v_pk_mul_f32 v[68:69], v[184:185], v[192:193]
	v_pk_mul_f32 v[70:71], v[186:187], v[194:195]
	v_pk_mul_f32 v[80:81], v[92:93], v[72:73]
	v_pk_mul_f32 v[82:83], v[94:95], v[74:75]
	v_pk_mul_f32 v[84:85], v[96:97], v[76:77]
	v_pk_mul_f32 v[86:87], v[98:99], v[78:79]
	v_pk_fma_f32 v[80:81], v[100:101], v[56:57], v[80:81]
	v_pk_fma_f32 v[82:83], v[102:103], v[58:59], v[82:83]
	v_pk_fma_f32 v[84:85], v[104:105], v[60:61], v[84:85]
	v_pk_fma_f32 v[86:87], v[106:107], v[62:63], v[86:87]
	v_pk_fma_f32 v[80:81], v[108:109], v[64:65], v[80:81]
	v_pk_fma_f32 v[82:83], v[110:111], v[66:67], v[82:83]
	v_pk_fma_f32 v[84:85], v[112:113], v[68:69], v[84:85]
	v_pk_fma_f32 v[86:87], v[114:115], v[70:71], v[86:87]
	s_waitcnt vmcnt(35)
	v_lshlrev_b32_e32 v196, 16, v136
	v_and_b32_e32 v197, 0xffff0000, v136
	v_lshlrev_b32_e32 v198, 16, v137
	v_and_b32_e32 v199, 0xffff0000, v137
	v_lshlrev_b32_e32 v200, 16, v138
	v_and_b32_e32 v201, 0xffff0000, v138
	v_lshlrev_b32_e32 v202, 16, v139
	v_and_b32_e32 v203, 0xffff0000, v139
	v_pk_mul_f32 v[80:81], v[80:81], v[196:197]
	v_pk_mul_f32 v[82:83], v[82:83], v[198:199]
	v_pk_mul_f32 v[84:85], v[84:85], v[200:201]
	v_pk_mul_f32 v[86:87], v[86:87], v[202:203]
	v_cvt_pk_bf16_f32 v212, v80, v81
	v_cvt_pk_bf16_f32 v213, v82, v83
	v_cvt_pk_bf16_f32 v214, v84, v85
	v_cvt_pk_bf16_f32 v215, v86, v87
	s_add_u32 s20, s26, 0x5000
	s_addc_u32 s21, s27, 0
	global_store_dwordx4 v220, v[212:215], s[20:21] offset:2048
	s_waitcnt vmcnt(11)
	v_lshlrev_b32_e32 v180, 16, v16
	v_and_b32_e32 v181, 0xffff0000, v16
	v_lshlrev_b32_e32 v182, 16, v17
	v_and_b32_e32 v183, 0xffff0000, v17
	v_lshlrev_b32_e32 v184, 16, v18
	v_and_b32_e32 v185, 0xffff0000, v18
	v_lshlrev_b32_e32 v186, 16, v19
	v_and_b32_e32 v187, 0xffff0000, v19
	v_lshlrev_b32_e32 v188, 16, v48
	v_and_b32_e32 v189, 0xffff0000, v48
	v_lshlrev_b32_e32 v190, 16, v49
	v_and_b32_e32 v191, 0xffff0000, v49
	v_lshlrev_b32_e32 v192, 16, v50
	v_and_b32_e32 v193, 0xffff0000, v50
	v_lshlrev_b32_e32 v194, 16, v51
	v_and_b32_e32 v195, 0xffff0000, v51
	v_pk_mul_f32 v[72:73], v[180:181], v[188:189]
	v_pk_mul_f32 v[74:75], v[182:183], v[190:191]
	v_pk_mul_f32 v[76:77], v[184:185], v[192:193]
	v_pk_mul_f32 v[78:79], v[186:187], v[194:195]
	v_pk_mul_f32 v[80:81], v[92:93], v[56:57]
	v_pk_mul_f32 v[82:83], v[94:95], v[58:59]
	v_pk_mul_f32 v[84:85], v[96:97], v[60:61]
	v_pk_mul_f32 v[86:87], v[98:99], v[62:63]
	v_pk_fma_f32 v[80:81], v[100:101], v[64:65], v[80:81]
	v_pk_fma_f32 v[82:83], v[102:103], v[66:67], v[82:83]
	v_pk_fma_f32 v[84:85], v[104:105], v[68:69], v[84:85]
	v_pk_fma_f32 v[86:87], v[106:107], v[70:71], v[86:87]
	v_pk_fma_f32 v[80:81], v[108:109], v[72:73], v[80:81]
	v_pk_fma_f32 v[82:83], v[110:111], v[74:75], v[82:83]
	v_pk_fma_f32 v[84:85], v[112:113], v[76:77], v[84:85]
	v_pk_fma_f32 v[86:87], v[114:115], v[78:79], v[86:87]
	s_waitcnt vmcnt(35)
	v_lshlrev_b32_e32 v196, 16, v140
	v_and_b32_e32 v197, 0xffff0000, v140
	v_lshlrev_b32_e32 v198, 16, v141
	v_and_b32_e32 v199, 0xffff0000, v141
	v_lshlrev_b32_e32 v200, 16, v142
	v_and_b32_e32 v201, 0xffff0000, v142
	v_lshlrev_b32_e32 v202, 16, v143
	v_and_b32_e32 v203, 0xffff0000, v143
	v_pk_mul_f32 v[80:81], v[80:81], v[196:197]
	v_pk_mul_f32 v[82:83], v[82:83], v[198:199]
	v_pk_mul_f32 v[84:85], v[84:85], v[200:201]
	v_pk_mul_f32 v[86:87], v[86:87], v[202:203]
	v_cvt_pk_bf16_f32 v208, v80, v81
	v_cvt_pk_bf16_f32 v209, v82, v83
	v_cvt_pk_bf16_f32 v210, v84, v85
	v_cvt_pk_bf16_f32 v211, v86, v87
	s_add_u32 s20, s26, 0x6000
	s_addc_u32 s21, s27, 0
	global_store_dwordx4 v220, v[208:211], s[20:21] offset:2048
	s_waitcnt vmcnt(9)
	v_lshlrev_b32_e32 v180, 16, v20
	v_and_b32_e32 v181, 0xffff0000, v20
	v_lshlrev_b32_e32 v182, 16, v21
	v_and_b32_e32 v183, 0xffff0000, v21
	v_lshlrev_b32_e32 v184, 16, v22
	v_and_b32_e32 v185, 0xffff0000, v22
	v_lshlrev_b32_e32 v186, 16, v23
	v_and_b32_e32 v187, 0xffff0000, v23
	v_lshlrev_b32_e32 v188, 16, v52
	v_and_b32_e32 v189, 0xffff0000, v52
	v_lshlrev_b32_e32 v190, 16, v53
	v_and_b32_e32 v191, 0xffff0000, v53
	v_lshlrev_b32_e32 v192, 16, v54
	v_and_b32_e32 v193, 0xffff0000, v54
	v_lshlrev_b32_e32 v194, 16, v55
	v_and_b32_e32 v195, 0xffff0000, v55
	v_pk_mul_f32 v[56:57], v[180:181], v[188:189]
	v_pk_mul_f32 v[58:59], v[182:183], v[190:191]
	v_pk_mul_f32 v[60:61], v[184:185], v[192:193]
	v_pk_mul_f32 v[62:63], v[186:187], v[194:195]
	v_pk_mul_f32 v[80:81], v[92:93], v[64:65]
	v_pk_mul_f32 v[82:83], v[94:95], v[66:67]
	v_pk_mul_f32 v[84:85], v[96:97], v[68:69]
	v_pk_mul_f32 v[86:87], v[98:99], v[70:71]
	v_pk_fma_f32 v[80:81], v[100:101], v[72:73], v[80:81]
	v_pk_fma_f32 v[82:83], v[102:103], v[74:75], v[82:83]
	v_pk_fma_f32 v[84:85], v[104:105], v[76:77], v[84:85]
	v_pk_fma_f32 v[86:87], v[106:107], v[78:79], v[86:87]
	v_pk_fma_f32 v[80:81], v[108:109], v[56:57], v[80:81]
	v_pk_fma_f32 v[82:83], v[110:111], v[58:59], v[82:83]
	v_pk_fma_f32 v[84:85], v[112:113], v[60:61], v[84:85]
	v_pk_fma_f32 v[86:87], v[114:115], v[62:63], v[86:87]
	s_waitcnt vmcnt(35)
	v_lshlrev_b32_e32 v196, 16, v144
	v_and_b32_e32 v197, 0xffff0000, v144
	v_lshlrev_b32_e32 v198, 16, v145
	v_and_b32_e32 v199, 0xffff0000, v145
	v_lshlrev_b32_e32 v200, 16, v146
	v_and_b32_e32 v201, 0xffff0000, v146
	v_lshlrev_b32_e32 v202, 16, v147
	v_and_b32_e32 v203, 0xffff0000, v147
	v_pk_mul_f32 v[80:81], v[80:81], v[196:197]
	v_pk_mul_f32 v[82:83], v[82:83], v[198:199]
	v_pk_mul_f32 v[84:85], v[84:85], v[200:201]
	v_pk_mul_f32 v[86:87], v[86:87], v[202:203]
	v_cvt_pk_bf16_f32 v212, v80, v81
	v_cvt_pk_bf16_f32 v213, v82, v83
	v_cvt_pk_bf16_f32 v214, v84, v85
	v_cvt_pk_bf16_f32 v215, v86, v87
	s_add_u32 s20, s26, 0x7000
	s_addc_u32 s21, s27, 0
	global_store_dwordx4 v220, v[212:215], s[20:21] offset:2048
	s_branch .LBB0_387

.LBB0_867:
	s_andn2_saveexec_b64 s[6:7], s[6:7]
	s_cbranch_execz .LBB0_897
	s_movk_i32 s1, 0x84
	v_lshlrev_b32_e32 v30, 2, v16
	global_load_dword v30, v30, s[64:65]
	v_mul_lo_u32 v0, v16, s1
	s_mov_b32 s9, 0
	v_add_u32_e32 v7, 0, v0
	v_mov_b32_e32 v8, 0
	v_mov_b32_e32 v4, 0xff61b1e6
	v_mov_b32_e32 v5, 0xff61b1e6
	v_mov_b32_e32 v6, 0xff61b1e6
	v_mov_b32_e32 v10, 0xff61b1e6
	v_mov_b32_e32 v0, 0
	v_mov_b32_e32 v3, 0
	v_mov_b32_e32 v1, 0
	v_mov_b32_e32 v2, 0
	s_mov_b32 s8, s9
	s_waitcnt vmcnt(0)
	v_mov_b32_e32 v9, v7
	ds_read_b32 v40, v9
	ds_read_b32 v41, v9 offset:4224
	ds_read_b32 v42, v9 offset:8448
	ds_read_b32 v43, v9 offset:12672
	ds_read_b32 v44, v9 offset:16896
	ds_read_b32 v45, v9 offset:21120
	ds_read_b32 v46, v9 offset:25344
	ds_read_b32 v47, v9 offset:29568
.Ltopk_loop:
	s_mov_b32 s2, s8
	v_readlane_b32 s3, v30, s2
	ds_read_b32 v48, v9 offset:4
	ds_read_b32 v49, v9 offset:4228
	ds_read_b32 v50, v9 offset:8452
	ds_read_b32 v51, v9 offset:12676
	ds_read_b32 v52, v9 offset:16900
	ds_read_b32 v53, v9 offset:21124
	ds_read_b32 v54, v9 offset:25348
	ds_read_b32 v55, v9 offset:29572
	s_waitcnt lgkmcnt(15)
	v_add_f32_e32 v11, s3, v40
	s_waitcnt lgkmcnt(14)
	v_add_f32_e32 v11, v11, v41
	s_waitcnt lgkmcnt(13)
	v_add_f32_e32 v11, v11, v42
	s_waitcnt lgkmcnt(12)
	v_add_f32_e32 v11, v11, v43
	s_waitcnt lgkmcnt(11)
	v_add_f32_e32 v11, v11, v44
	s_waitcnt lgkmcnt(10)
	v_add_f32_e32 v11, v11, v45
	s_waitcnt lgkmcnt(9)
	v_add_f32_e32 v11, v11, v46
	s_waitcnt lgkmcnt(8)
	v_add_f32_e32 v11, v11, v47
	v_cmp_gt_f32_e64 s[10:11], v11, v10
	v_cmp_gt_f32_e64 s[12:13], v11, v6
	v_cmp_gt_f32_e64 s[14:15], v11, v5
	v_cmp_gt_f32_e64 s[16:17], v11, v4
	v_mov_b32_e32 v12, s2
	v_cndmask_b32_e64 v10, v10, v11, s[10:11]
	v_cndmask_b32_e64 v10, v10, v6, s[12:13]
	v_cndmask_b32_e64 v3, v3, v12, s[10:11]
	v_cndmask_b32_e64 v3, v3, v2, s[12:13]
	v_cndmask_b32_e64 v6, v6, v11, s[12:13]
	v_cndmask_b32_e64 v6, v6, v5, s[14:15]
	v_cndmask_b32_e64 v2, v2, v12, s[12:13]
	v_cndmask_b32_e64 v2, v2, v1, s[14:15]
	v_cndmask_b32_e64 v5, v5, v11, s[14:15]
	v_cndmask_b32_e64 v5, v5, v4, s[16:17]
	v_cndmask_b32_e64 v1, v1, v12, s[14:15]
	v_cndmask_b32_e64 v1, v1, v0, s[16:17]
	v_cndmask_b32_e64 v4, v4, v11, s[16:17]
	v_cndmask_b32_e64 v0, v0, v12, s[16:17]
	s_add_i32 s2, s8, 1
	v_readlane_b32 s3, v30, s2
	ds_read_b32 v40, v9 offset:8
	ds_read_b32 v41, v9 offset:4232
	ds_read_b32 v42, v9 offset:8456
	ds_read_b32 v43, v9 offset:12680
	ds_read_b32 v44, v9 offset:16904
	ds_read_b32 v45, v9 offset:21128
	ds_read_b32 v46, v9 offset:25352
	ds_read_b32 v47, v9 offset:29576
	s_waitcnt lgkmcnt(15)
	v_add_f32_e32 v11, s3, v48
	s_waitcnt lgkmcnt(14)
	v_add_f32_e32 v11, v11, v49
	s_waitcnt lgkmcnt(13)
	v_add_f32_e32 v11, v11, v50
	s_waitcnt lgkmcnt(12)
	v_add_f32_e32 v11, v11, v51
	s_waitcnt lgkmcnt(11)
	v_add_f32_e32 v11, v11, v52
	s_waitcnt lgkmcnt(10)
	v_add_f32_e32 v11, v11, v53
	s_waitcnt lgkmcnt(9)
	v_add_f32_e32 v11, v11, v54
	s_waitcnt lgkmcnt(8)
	v_add_f32_e32 v11, v11, v55
	v_cmp_gt_f32_e64 s[10:11], v11, v10
	v_cmp_gt_f32_e64 s[12:13], v11, v6
	v_cmp_gt_f32_e64 s[14:15], v11, v5
	v_cmp_gt_f32_e64 s[16:17], v11, v4
	v_mov_b32_e32 v12, s2
	v_cndmask_b32_e64 v10, v10, v11, s[10:11]
	v_cndmask_b32_e64 v10, v10, v6, s[12:13]
	v_cndmask_b32_e64 v3, v3, v12, s[10:11]
	v_cndmask_b32_e64 v3, v3, v2, s[12:13]
	v_cndmask_b32_e64 v6, v6, v11, s[12:13]
	v_cndmask_b32_e64 v6, v6, v5, s[14:15]
	v_cndmask_b32_e64 v2, v2, v12, s[12:13]
	v_cndmask_b32_e64 v2, v2, v1, s[14:15]
	v_cndmask_b32_e64 v5, v5, v11, s[14:15]
	v_cndmask_b32_e64 v5, v5, v4, s[16:17]
	v_cndmask_b32_e64 v1, v1, v12, s[14:15]
	v_cndmask_b32_e64 v1, v1, v0, s[16:17]
	v_cndmask_b32_e64 v4, v4, v11, s[16:17]
	v_cndmask_b32_e64 v0, v0, v12, s[16:17]
	s_add_i32 s2, s8, 2
	v_readlane_b32 s3, v30, s2
	ds_read_b32 v48, v9 offset:12
	ds_read_b32 v49, v9 offset:4236
	ds_read_b32 v50, v9 offset:8460
	ds_read_b32 v51, v9 offset:12684
	ds_read_b32 v52, v9 offset:16908
	ds_read_b32 v53, v9 offset:21132
	ds_read_b32 v54, v9 offset:25356
	ds_read_b32 v55, v9 offset:29580
	s_waitcnt lgkmcnt(15)
	v_add_f32_e32 v11, s3, v40
	s_waitcnt lgkmcnt(14)
	v_add_f32_e32 v11, v11, v41
	s_waitcnt lgkmcnt(13)
	v_add_f32_e32 v11, v11, v42
	s_waitcnt lgkmcnt(12)
	v_add_f32_e32 v11, v11, v43
	s_waitcnt lgkmcnt(11)
	v_add_f32_e32 v11, v11, v44
	s_waitcnt lgkmcnt(10)
	v_add_f32_e32 v11, v11, v45
	s_waitcnt lgkmcnt(9)
	v_add_f32_e32 v11, v11, v46
	s_waitcnt lgkmcnt(8)
	v_add_f32_e32 v11, v11, v47
	v_cmp_gt_f32_e64 s[10:11], v11, v10
	v_cmp_gt_f32_e64 s[12:13], v11, v6
	v_cmp_gt_f32_e64 s[14:15], v11, v5
	v_cmp_gt_f32_e64 s[16:17], v11, v4
	v_mov_b32_e32 v12, s2
	v_cndmask_b32_e64 v10, v10, v11, s[10:11]
	v_cndmask_b32_e64 v10, v10, v6, s[12:13]
	v_cndmask_b32_e64 v3, v3, v12, s[10:11]
	v_cndmask_b32_e64 v3, v3, v2, s[12:13]
	v_cndmask_b32_e64 v6, v6, v11, s[12:13]
	v_cndmask_b32_e64 v6, v6, v5, s[14:15]
	v_cndmask_b32_e64 v2, v2, v12, s[12:13]
	v_cndmask_b32_e64 v2, v2, v1, s[14:15]
	v_cndmask_b32_e64 v5, v5, v11, s[14:15]
	v_cndmask_b32_e64 v5, v5, v4, s[16:17]
	v_cndmask_b32_e64 v1, v1, v12, s[14:15]
	v_cndmask_b32_e64 v1, v1, v0, s[16:17]
	v_cndmask_b32_e64 v4, v4, v11, s[16:17]
	v_cndmask_b32_e64 v0, v0, v12, s[16:17]
	s_add_i32 s2, s8, 3
	v_readlane_b32 s3, v30, s2
	ds_read_b32 v40, v9 offset:16
	ds_read_b32 v41, v9 offset:4240
	ds_read_b32 v42, v9 offset:8464
	ds_read_b32 v43, v9 offset:12688
	ds_read_b32 v44, v9 offset:16912
	ds_read_b32 v45, v9 offset:21136
	ds_read_b32 v46, v9 offset:25360
	ds_read_b32 v47, v9 offset:29584
	s_waitcnt lgkmcnt(15)
	v_add_f32_e32 v11, s3, v48
	s_waitcnt lgkmcnt(14)
	v_add_f32_e32 v11, v11, v49
	s_waitcnt lgkmcnt(13)
	v_add_f32_e32 v11, v11, v50
	s_waitcnt lgkmcnt(12)
	v_add_f32_e32 v11, v11, v51
	s_waitcnt lgkmcnt(11)
	v_add_f32_e32 v11, v11, v52
	s_waitcnt lgkmcnt(10)
	v_add_f32_e32 v11, v11, v53
	s_waitcnt lgkmcnt(9)
	v_add_f32_e32 v11, v11, v54
	s_waitcnt lgkmcnt(8)
	v_add_f32_e32 v11, v11, v55
	v_cmp_gt_f32_e64 s[10:11], v11, v10
	v_cmp_gt_f32_e64 s[12:13], v11, v6
	v_cmp_gt_f32_e64 s[14:15], v11, v5
	v_cmp_gt_f32_e64 s[16:17], v11, v4
	v_mov_b32_e32 v12, s2
	v_cndmask_b32_e64 v10, v10, v11, s[10:11]
	v_cndmask_b32_e64 v10, v10, v6, s[12:13]
	v_cndmask_b32_e64 v3, v3, v12, s[10:11]
	v_cndmask_b32_e64 v3, v3, v2, s[12:13]
	v_cndmask_b32_e64 v6, v6, v11, s[12:13]
	v_cndmask_b32_e64 v6, v6, v5, s[14:15]
	v_cndmask_b32_e64 v2, v2, v12, s[12:13]
	v_cndmask_b32_e64 v2, v2, v1, s[14:15]
	v_cndmask_b32_e64 v5, v5, v11, s[14:15]
	v_cndmask_b32_e64 v5, v5, v4, s[16:17]
	v_cndmask_b32_e64 v1, v1, v12, s[14:15]
	v_cndmask_b32_e64 v1, v1, v0, s[16:17]
	v_cndmask_b32_e64 v4, v4, v11, s[16:17]
	v_cndmask_b32_e64 v0, v0, v12, s[16:17]
	v_add_u32_e32 v9, 16, v9
	s_add_i32 s8, s8, 4
	s_cmp_eq_u32 s8, 32
	s_cbranch_scc0 .Ltopk_loop
